# MLA phase-entry stagger (8 groups x 0.75us) on top of v68
# baseline (speedup 1.0000x reference)
.LBB0_687:
	v_writelane_b32 v255, s75, 30
	v_writelane_b32 v255, s76, 9
	s_nop 1
	v_writelane_b32 v255, s77, 10
	s_or_b64 exec, exec, s[0:1]
	s_mov_b32 s72, s73
	v_readlane_b32 s5, v254, 4
	v_readlane_b32 s0, v254, 2
	s_waitcnt lgkmcnt(0)
	s_barrier
	s_lshr_b32 s98, s5, 3
	s_and_b32 s98, s98, 7
	s_cmp_eq_u32 s98, 0
	s_cbranch_scc1 .Lstgm_done
.Lstgm_loop:
	s_sleep 28
	s_add_i32 s98, s98, -1
	s_cmp_lg_u32 s98, 0
	s_cbranch_scc1 .Lstgm_loop
.Lstgm_done:
	s_cmpk_lt_i32 s5, 0x100
	v_writelane_b32 v255, s0, 50
	v_readlane_b32 s0, v254, 3
	s_cbranch_scc0 .LBB0_853
	v_readlane_b32 s0, v254, 15
	v_readlane_b32 s2, v254, 17
	v_readlane_b32 s1, v254, 16
	v_readlane_b32 s3, v254, 18
	s_add_u32 s0, s2, s72
	s_addc_u32 s1, s3, 0
	s_add_u32 s2, s0, 0x12000000
	v_writelane_b32 v255, s2, 52
	s_addc_u32 s2, s1, 0
	v_writelane_b32 v255, s2, 40
	s_add_u32 s2, s0, 0x15000000
	v_writelane_b32 v255, s2, 38
	s_addc_u32 s2, s1, 0
	v_writelane_b32 v255, s2, 36
	s_add_u32 s2, s0, 0xc8000000
	v_writelane_b32 v255, s2, 44
	s_addc_u32 s2, s1, 0
	v_writelane_b32 v255, s2, 46
	s_add_u32 s0, s0, 0xa000000
	v_writelane_b32 v255, s0, 34
	s_addc_u32 s0, s1, 0
	v_writelane_b32 v255, s0, 32
	s_branch .LBB0_690
